# P2 stage D2 (wave 6 column block): three serialised tile reads issued together; stacked on stage B/D1/D2/G/H/I pipelining
# baseline (speedup 1.0000x reference)
.LBB0_447:
	s_movk_i32 s70, 0x180
	s_movk_i32 s71, 0x80
	s_andn2_b64 vcc, exec, s[60:61]
	s_cbranch_vccnz .LBB0_456
	v_and_b32_e32 v8, 15, v186
	v_readlane_b32 s10, v254, 8
	v_lshrrev_b32_e32 v2, 4, v2
	v_lshl_add_u32 v4, v8, 8, s18
	s_cmp_lt_i32 s10, 5
	s_mov_b64 s[92:93], -1
	s_cbranch_scc1 .LBB0_454
	v_readlane_b32 s10, v254, 8
	s_cmp_lg_u32 s10, 5
	s_cbranch_scc0 .LBB0_451
	v_and_b32_e32 v1, 48, v186
	v_add_u32_e32 v5, v4, v1
	v_lshlrev_b32_e32 v252, 6, v8
	v_add3_u32 v1, s25, v252, v1
	v_lshlrev_b32_e32 v9, 2, v2
	s_add_i32 s10, 0, 0x18000
	v_or_b32_e32 v252, 32, v8
	v_lshlrev_b32_e32 v253, 6, v252
	v_lshlrev_b32_e32 v10, 4, v2
	v_add3_u32 v253, s22, v253, v10
	ds_read_b128 v[228:231], v5 offset:12416
	ds_read_b128 v[232:235], v1 offset:3072
	ds_read_b128 v[236:239], v253
	v_lshrrev_b32_e32 v1, 3, v252
	s_mov_b64 s[92:93], 0
	v_lshlrev_b32_e32 v5, 1, v186
	v_and_b32_e32 v5, 14, v5
	s_waitcnt lgkmcnt(2)
	v_cvt_pk_bf16_f32 v6, v228, v229
	v_cvt_pk_bf16_f32 v7, v230, v231
	s_waitcnt lgkmcnt(1)
	v_cvt_pk_bf16_f32 v14, v232, v233
	v_cvt_pk_bf16_f32 v15, v234, v235
	s_waitcnt lgkmcnt(0)
	v_cvt_pk_bf16_f32 v10, v236, v237
	v_cvt_pk_bf16_f32 v11, v238, v239
	s_nop 1
	v_mfma_f32_16x16x16_bf16 v[10:13], v[6:7], v[10:11], 0
	s_nop 7
	v_cvt_pk_bf16_f32 v6, v10, v11
	v_cvt_pk_bf16_f32 v7, v12, v13
	s_nop 1
	v_mfma_f32_16x16x16_bf16 v[10:13], v[14:15], v[6:7], 0
	s_nop 7
	v_xor_b32_e32 v6, 0x80000000, v10
	v_bfe_u32 v7, v6, 16, 1
	v_bitop3_b32 v10, v9, v1, 4 bitop3:0x6c
	v_add3_u32 v6, v6, v7, s19
	v_lshlrev_b32_e32 v7, 9, v2
	v_lshl_add_u32 v10, v10, 4, s10
	v_add3_u32 v7, v10, v7, v5
	ds_write_b16_d16_hi v7, v6 offset:6144
	v_xor_b32_e32 v7, 0x80000000, v11
	v_or_b32_e32 v6, 1, v9
	v_bfe_u32 v10, v7, 16, 1
	v_add3_u32 v7, v7, v10, s19
	v_lshlrev_b32_e32 v10, 7, v6
	v_bitop3_b32 v6, v6, v1, 5 bitop3:0x6c
	v_lshl_add_u32 v6, v6, 4, s10
	v_add3_u32 v6, v6, v10, v5
	ds_write_b16_d16_hi v6, v7 offset:6144
	v_xor_b32_e32 v7, 0x80000000, v12
	v_or_b32_e32 v6, 2, v9
	v_bfe_u32 v10, v7, 16, 1
	v_add3_u32 v7, v7, v10, s19
	v_lshlrev_b32_e32 v10, 7, v6
	v_bitop3_b32 v6, v6, v1, 6 bitop3:0x6c
	v_lshl_add_u32 v6, v6, 4, s10
	v_add3_u32 v6, v6, v10, v5
	ds_write_b16_d16_hi v6, v7 offset:6144
	v_or_b32_e32 v6, 3, v9
	v_xor_b32_e32 v7, 0x80000000, v13
	v_bfe_u32 v9, v7, 16, 1
	v_bitop3_b32 v1, v6, v1, 7 bitop3:0x6c
	v_add3_u32 v7, v7, v9, s19
	v_lshlrev_b32_e32 v9, 7, v6
	v_lshl_add_u32 v1, v1, 4, s10
	v_add3_u32 v1, v1, v9, v5
	ds_write_b16_d16_hi v1, v7 offset:6144
